# speedup vs baseline: 1.0602x; 1.0028x over previous
.LBB1_5:
	s_waitcnt lgkmcnt(6)
	v_mfma_f32_32x32x64_f8f6f4 v[4:19], v[156:163], v[148:155], v[4:19]
	v_cmp_eq_u32_e32 vcc, 0, v1
	s_nop 1
	s_and_saveexec_b64 s[0:1], vcc
	s_lshl_b32 s12, s29, 2
	s_add_i32 s12, s12, 0x12000
	v_mov_b32_e32 v1, s12
	ds_write_b32 v1, v0
	s_or_b64 exec, exec, s[0:1]
	s_waitcnt vmcnt(0) lgkmcnt(0)
	s_barrier
	s_waitcnt lgkmcnt(4)
	v_mfma_f32_32x32x64_f8f6f4 v[20:35], v[164:171], v[148:155], v[20:35]
	s_waitcnt lgkmcnt(1)
	v_mfma_f32_32x32x64_f8f6f4 v[4:19], v[80:87], v[72:79], v[4:19]
	v_mov_b32_e32 v104, 0x12000
	ds_read_b128 v[38:41], v104
	ds_read_b128 v[42:45], v104 offset:16
	s_mov_b32 s14, 0
	s_waitcnt lgkmcnt(0)
	v_or_b32_e32 v0, v39, v38
	v_or_b32_e32 v0, v40, v0
	v_or_b32_e32 v0, v41, v0
	v_or_b32_e32 v0, v42, v0
	v_or_b32_e32 v0, v43, v0
	v_or_b32_e32 v0, v44, v0
	v_or_b32_e32 v0, v45, v0
	v_mfma_f32_32x32x64_f8f6f4 v[20:35], v[58:65], v[72:79], v[20:35]
	v_cmp_ne_u32_e32 vcc, 0, v0
	s_cbranch_vccnz .LBB1_13
	s_mov_b64 s[0:1], -1
	s_nop 2
	v_mov_b64_e32 v[54:55], v[4:5]
	v_mov_b64_e32 v[56:57], v[6:7]
	v_mov_b64_e32 v[58:59], v[8:9]
	v_mov_b64_e32 v[60:61], v[10:11]
	v_mov_b64_e32 v[62:63], v[12:13]
	v_mov_b64_e32 v[64:65], v[14:15]
	v_mov_b64_e32 v[66:67], v[16:17]
	v_mov_b64_e32 v[68:69], v[18:19]
	s_nop 5
	v_mov_b64_e32 v[38:39], v[20:21]
	v_mov_b64_e32 v[40:41], v[22:23]
	v_mov_b64_e32 v[42:43], v[24:25]
	v_mov_b64_e32 v[44:45], v[26:27]
	v_mov_b64_e32 v[46:47], v[28:29]
	v_mov_b64_e32 v[48:49], v[30:31]
	v_mov_b64_e32 v[50:51], v[32:33]
	v_mov_b64_e32 v[52:53], v[34:35]
	s_branch .Lfinal_copy
